# speedup vs baseline: 1.0409x; 1.0409x over previous
.LBB0_78:
	s_or_b64 exec, exec, s[0:1]
	v_readfirstlane_b32 s0, v63
	s_lshl_b32 s1, s0, 2
	s_waitcnt vmcnt(0)
	s_setprio 3
	v_pk_add_f32 v[82:83], v[16:17], v[20:21]
	v_pk_add_f32 v[84:85], v[14:15], v[18:19]
	s_waitcnt vmcnt(0)
	v_pk_add_f32 v[88:89], v[24:25], v[28:29]
	v_pk_add_f32 v[90:91], v[22:23], v[26:27]
	s_and_b32 s1, s1, 60
	s_ashr_i32 s24, s0, 4
	v_pk_add_f32 v[82:83], v[82:83], v[88:89]
	v_pk_add_f32 v[84:85], v[84:85], v[90:91]
	v_pk_add_f32 v[88:89], v[32:33], v[36:37]
	v_pk_add_f32 v[90:91], v[30:31], v[34:35]
	v_pk_add_f32 v[92:93], v[40:41], v[44:45]
	v_pk_add_f32 v[94:95], v[38:39], v[42:43]
	s_add_i32 s24, s24, s1
	v_pk_add_f32 v[88:89], v[88:89], v[92:93]
	v_pk_add_f32 v[90:91], v[90:91], v[94:95]
	v_pk_add_f32 v[92:93], v[48:49], v[52:53]
	v_pk_add_f32 v[94:95], v[46:47], v[50:51]
	v_pk_add_f32 v[96:97], v[56:57], v[60:61]
	v_pk_add_f32 v[98:99], v[54:55], v[58:59]
	s_add_i32 s24, s24, 1
	v_pk_add_f32 v[92:93], v[92:93], v[96:97]
	v_pk_add_f32 v[94:95], v[94:95], v[98:99]
	v_pk_add_f32 v[96:97], v[68:69], v[72:73]
	v_pk_add_f32 v[98:99], v[66:67], v[70:71]
	v_pk_add_f32 v[100:101], v[76:77], v[80:81]
	v_pk_add_f32 v[102:103], v[74:75], v[78:79]
	s_cmp_lt_i32 s0, 48
	v_pk_add_f32 v[96:97], v[96:97], v[100:101]
	v_pk_add_f32 v[98:99], v[98:99], v[102:103]
	s_mul_i32 s0, s34, 0x110
	v_add_u32_e32 v63, 0xb000, v107
	v_pk_add_f32 v[86:87], v[6:7], v[10:11]
	v_pk_add_f32 v[82:83], v[82:83], v[88:89]
	v_pk_add_f32 v[84:85], v[84:85], v[90:91]
	v_pk_add_f32 v[88:89], v[92:93], v[96:97]
	v_pk_add_f32 v[90:91], v[94:95], v[98:99]
	v_add_u32_e32 v63, s0, v63
	v_pk_add_f32 v[88:89], v[82:83], v[88:89]
	v_pk_add_f32 v[98:99], v[84:85], v[90:91]
	ds_read_b128 v[82:85], v63
	v_mov_b32_e32 v63, v86
	s_nop 1
	v_permlane16_swap_b32_e32 v86, v63
	v_add_f32_e32 v90, v86, v63
	v_mov_b32_e32 v63, v87
	v_pk_add_f32 v[64:65], v[8:9], v[12:13]
	s_nop 0
	v_permlane16_swap_b32_e32 v87, v63
	v_add_f32_e32 v91, v87, v63
	v_mov_b32_e32 v63, v64
	s_nop 1
	v_permlane16_swap_b32_e32 v64, v63
	v_add_f32_e32 v94, v64, v63
	v_mov_b32_e32 v63, v65
	s_nop 1
	v_permlane16_swap_b32_e32 v65, v63
	v_add_f32_e32 v95, v65, v63
	v_mov_b32_e32 v63, v98
	s_nop 1
	v_permlane16_swap_b32_e32 v98, v63
	v_add_f32_e32 v98, v98, v63
	v_mov_b32_e32 v63, v99
	s_nop 1
	v_permlane16_swap_b32_e32 v99, v63
	v_add_f32_e32 v99, v99, v63
	v_mov_b32_e32 v63, v88
	s_nop 1
	v_permlane16_swap_b32_e32 v88, v63
	v_add_f32_e32 v102, v88, v63
	v_mov_b32_e32 v63, v89
	ds_bpermute_b32 v118, v108, v2
	ds_bpermute_b32 v115, v108, v3
	ds_bpermute_b32 v114, v108, v4
	ds_bpermute_b32 v127, v108, v5
	ds_bpermute_b32 v124, v109, v2
	ds_bpermute_b32 v126, v109, v3
	ds_bpermute_b32 v125, v109, v4
	ds_bpermute_b32 v123, v109, v5
	ds_bpermute_b32 v120, v110, v2
	ds_bpermute_b32 v122, v110, v3
	ds_bpermute_b32 v121, v110, v4
	ds_bpermute_b32 v119, v110, v5
	v_permlane16_swap_b32_e32 v89, v63
	v_add_f32_e32 v103, v89, v63
	v_mov_b32_e32 v92, v90
	v_mov_b32_e32 v93, v91
	v_mov_b32_e32 v96, v94
	v_mov_b32_e32 v97, v95
	v_mov_b32_e32 v100, v98
	v_mov_b32_e32 v101, v99
	v_mov_b32_e32 v104, v102
	v_mov_b32_e32 v105, v103
	s_cselect_b32 s25, s24, -1
	v_permlane32_swap_b32_e32 v90, v92
	v_permlane32_swap_b32_e32 v91, v93
	v_permlane32_swap_b32_e32 v94, v96
	v_permlane32_swap_b32_e32 v95, v97
	v_permlane32_swap_b32_e32 v98, v100
	v_permlane32_swap_b32_e32 v99, v101
	v_permlane32_swap_b32_e32 v102, v104
	v_permlane32_swap_b32_e32 v103, v105
	s_cmp_lt_i32 s25, 0
	s_mov_b32 s26, s36
	s_mov_b32 s27, s35
	s_cbranch_scc1 .LBB0_118
	s_lshl_b32 s0, s25, 5
	s_add_i32 s37, s0, 0x14400
	v_mov_b32_e32 v2, s37
	ds_read_b128 v[8:11], v2
	v_add_u32_e32 v2, s0, v111
	ds_read2_b32 v[14:15], v2 offset1:4
	v_mov_b32_e32 v6, v62
	v_mov_b32_e32 v7, v62
	s_waitcnt lgkmcnt(1)
	v_readfirstlane_b32 s27, v8
	v_readfirstlane_b32 s26, v9
	v_mov_b32_e32 v8, v62
	v_mov_b32_e32 v9, v62
	v_mov_b64_e32 v[2:3], v[6:7]
	v_mov_b64_e32 v[4:5], v[8:9]
	s_and_saveexec_b64 s[0:1], s[16:17]
	s_cbranch_execz .LBB0_81
	v_mov_b32_e32 v2, s37
	ds_read_b32 v2, v2 offset:16
	v_mov_b32_e32 v3, v62
	s_waitcnt lgkmcnt(0)
	v_cndmask_b32_e64 v2, v2, v11, s[12:13]
	v_cndmask_b32_e64 v2, v2, v10, s[14:15]
	v_lshl_or_b32 v2, v2, 8, v107
	v_lshl_add_u64 v[2:3], v[0:1], 0, v[2:3]
	global_load_dwordx4 v[2:5], v[2:3], off sc0 nt

.LBB0_118:
	s_setprio 0
	s_max_i32 s0, s36, 1
	v_cvt_f32_u32_e32 v63, s0
	v_pk_add_f32 v[64:65], v[90:91], v[92:93]
	s_waitcnt lgkmcnt(0)
	v_pk_add_f32 v[86:87], v[94:95], v[96:97]
	v_pk_add_f32 v[88:89], v[98:99], v[100:101]
	v_div_scale_f32 v92, s[0:1], v63, v63, 1.0
	v_rcp_f32_e32 v93, v92
	s_max_i32 s0, s35, 1
	v_pk_add_f32 v[90:91], v[102:103], v[104:105]
	v_mul_f32_e32 v99, v83, v126
	v_fma_f32 v94, -v92, v93, 1.0
	v_fmac_f32_e32 v93, v94, v93
	v_div_scale_f32 v94, vcc, 1.0, v63, 1.0
	v_mul_f32_e32 v95, v94, v93
	v_fma_f32 v96, -v92, v95, v94
	v_fmac_f32_e32 v95, v96, v93
	v_fma_f32 v92, -v92, v95, v94
	v_div_fmas_f32 v92, v92, v93, v95
	v_div_fixup_f32 v92, v92, v63, 1.0
	v_cvt_f32_u32_e32 v63, s0
	v_mul_f32_e32 v102, v83, v122
	v_fmac_f32_e32 v99, v82, v124
	v_fmac_f32_e32 v102, v82, v120
	v_div_scale_f32 v93, s[0:1], v63, v63, 1.0
	v_rcp_f32_e32 v94, v93
	v_fmac_f32_e32 v99, v84, v125
	v_fmac_f32_e32 v102, v84, v121
	v_fmac_f32_e32 v99, v85, v123
	v_fma_f32 v95, -v93, v94, 1.0
	v_fmac_f32_e32 v94, v95, v94
	v_div_scale_f32 v95, vcc, 1.0, v63, 1.0
	v_mul_f32_e32 v96, v95, v94
	v_fma_f32 v97, -v93, v96, v95
	v_fmac_f32_e32 v96, v97, v94
	v_fma_f32 v93, -v93, v96, v95
	v_div_fmas_f32 v93, v93, v94, v96
	v_div_fixup_f32 v94, v93, v63, 1.0
	v_pk_mul_f32 v[64:65], v[92:93], v[64:65] op_sel_hi:[0,1]
	v_pk_mul_f32 v[88:89], v[94:95], v[88:89] op_sel_hi:[0,1]
	v_pk_mul_f32 v[86:87], v[92:93], v[86:87] op_sel_hi:[0,1]
	v_mul_f32_e32 v93, v65, v115
	v_mul_f32_e32 v97, v65, v126
	v_mul_f32_e32 v100, v65, v122
	v_mul_f32_e32 v103, v65, v89
	v_mul_f32_e32 v65, v83, v65
	v_mul_f32_e32 v63, v115, v126
	v_fmac_f32_e32 v93, v64, v118
	v_fmac_f32_e32 v97, v64, v124
	v_fmac_f32_e32 v100, v64, v120
	v_fmac_f32_e32 v103, v64, v88
	v_fmac_f32_e32 v65, v82, v64
	v_mul_f32_e32 v64, v83, v89
	v_pk_mul_f32 v[90:91], v[94:95], v[90:91] op_sel_hi:[0,1]
	v_fmac_f32_e32 v63, v118, v124
	v_mul_f32_e32 v92, v115, v122
	v_mul_f32_e32 v94, v89, v115
	v_mul_f32_e32 v95, v83, v115
	v_mul_f32_e32 v96, v126, v122
	v_mul_f32_e32 v98, v89, v126
	v_mul_f32_e32 v101, v89, v122
	v_fmac_f32_e32 v64, v82, v88
	v_fmac_f32_e32 v63, v114, v125
	v_fmac_f32_e32 v92, v118, v120
	v_fmac_f32_e32 v94, v88, v118
	v_fmac_f32_e32 v95, v82, v118
	v_fmac_f32_e32 v96, v124, v120
	v_fmac_f32_e32 v98, v88, v124
	v_fmac_f32_e32 v101, v88, v120
	v_fmac_f32_e32 v65, v84, v86
	v_fmac_f32_e32 v64, v84, v90
	v_fmac_f32_e32 v63, v127, v123
	v_fmac_f32_e32 v92, v114, v121
	v_fmac_f32_e32 v93, v86, v114
	v_fmac_f32_e32 v94, v90, v114
	v_fmac_f32_e32 v95, v84, v114
	v_fmac_f32_e32 v96, v125, v121
	v_fmac_f32_e32 v97, v86, v125
	v_fmac_f32_e32 v98, v90, v125
	v_fmac_f32_e32 v100, v86, v121
	v_fmac_f32_e32 v101, v90, v121
	v_fmac_f32_e32 v103, v86, v90
	v_fmac_f32_e32 v65, v85, v87
	v_fmac_f32_e32 v64, v85, v91
	v_fmac_f32_e32 v92, v127, v119
	v_fmac_f32_e32 v93, v87, v127
	v_fmac_f32_e32 v94, v91, v127
	v_fmac_f32_e32 v95, v85, v127
	v_fmac_f32_e32 v96, v123, v119
	v_fmac_f32_e32 v97, v87, v123
	v_fmac_f32_e32 v98, v91, v123
	v_fmac_f32_e32 v100, v87, v119
	v_fmac_f32_e32 v101, v91, v119
	v_fmac_f32_e32 v102, v85, v119
	v_fmac_f32_e32 v103, v87, v91
	v_cndmask_b32_e64 v82, v63, v99, s[4:5]
	v_cndmask_b32_e64 v63, v99, v63, s[4:5]
	v_cndmask_b32_e64 v83, v100, v92, s[4:5]
	v_cndmask_b32_e64 v84, v101, v93, s[4:5]
	v_add_f32_dpp v63, v82, v63 row_ror:8 row_mask:0xf bank_mask:0xf bound_ctrl:1
	v_cndmask_b32_e64 v82, v92, v100, s[4:5]
	v_cndmask_b32_e64 v85, v102, v94, s[4:5]
	v_cndmask_b32_e64 v86, v103, v95, s[4:5]
	v_add_f32_dpp v82, v82, v83 row_ror:8 row_mask:0xf bank_mask:0xf bound_ctrl:1
	v_cndmask_b32_e64 v83, v93, v101, s[4:5]
	v_cndmask_b32_e64 v87, 0, v98, s[4:5]
	s_nop 0
	v_add_f32_dpp v83, v83, v84 row_ror:8 row_mask:0xf bank_mask:0xf bound_ctrl:1
	v_cndmask_b32_e64 v84, v94, v102, s[4:5]
	s_nop 1
	v_add_f32_dpp v84, v84, v85 row_ror:8 row_mask:0xf bank_mask:0xf bound_ctrl:1
	v_cndmask_b32_e64 v85, v95, v103, s[4:5]
	s_nop 1
	v_add_f32_dpp v85, v85, v86 row_ror:8 row_mask:0xf bank_mask:0xf bound_ctrl:1
	v_cndmask_b32_e64 v86, v96, v65, s[4:5]
	v_cndmask_b32_e64 v65, v65, v96, s[4:5]
	s_nop 1
	v_add_f32_dpp v65, v86, v65 row_ror:8 row_mask:0xf bank_mask:0xf bound_ctrl:1
	v_cndmask_b32_e64 v86, v97, v64, s[4:5]
	v_cndmask_b32_e64 v64, v64, v97, s[4:5]
	s_nop 1
	v_add_f32_dpp v64, v86, v64 row_ror:8 row_mask:0xf bank_mask:0xf bound_ctrl:1
	v_cndmask_b32_e64 v86, v98, 0, s[4:5]
	s_nop 1
	v_add_f32_dpp v86, v86, v87 row_ror:8 row_mask:0xf bank_mask:0xf bound_ctrl:1
	v_cndmask_b32_e64 v87, v63, v85, s[6:7]
	v_cndmask_b32_e64 v63, v85, v63, s[6:7]
	v_cndmask_b32_e64 v85, v82, v65, s[6:7]
	v_cndmask_b32_e64 v65, v65, v82, s[6:7]
	v_cndmask_b32_e64 v82, v83, v64, s[6:7]
	v_cndmask_b32_e64 v64, v64, v83, s[6:7]
	v_cndmask_b32_e64 v83, v86, v84, s[6:7]
	v_add_f32_dpp v63, v87, v63 row_half_mirror row_mask:0xf bank_mask:0xf bound_ctrl:1
	v_add_f32_dpp v64, v82, v64 row_half_mirror row_mask:0xf bank_mask:0xf bound_ctrl:1
	v_cndmask_b32_e64 v82, v84, v86, s[6:7]
	v_add_f32_dpp v65, v85, v65 row_half_mirror row_mask:0xf bank_mask:0xf bound_ctrl:1
	s_nop 0
	v_add_f32_dpp v82, v82, v83 row_half_mirror row_mask:0xf bank_mask:0xf bound_ctrl:1
	v_cndmask_b32_e64 v83, v63, v64, s[8:9]
	v_cndmask_b32_e64 v63, v64, v63, s[8:9]
	v_cndmask_b32_e64 v64, v65, v82, s[8:9]
	v_cndmask_b32_e64 v65, v82, v65, s[8:9]
	v_add_f32_dpp v63, v83, v63 quad_perm:[2,3,0,1] row_mask:0xf bank_mask:0xf bound_ctrl:1
	s_nop 0
	v_add_f32_dpp v64, v64, v65 quad_perm:[2,3,0,1] row_mask:0xf bank_mask:0xf bound_ctrl:1
	v_cndmask_b32_e64 v82, v63, v64, s[10:11]
	v_mov_b32_e32 v65, v62
	s_nop 1
	v_mov_b32_dpp v65, v82 quad_perm:[1,0,3,2] row_mask:0xf bank_mask:0xf
	s_and_saveexec_b64 s[0:1], s[14:15]
	s_cbranch_execz .LBB0_73
	v_cndmask_b32_e64 v63, v64, v63, s[10:11]
	v_add_f32_e32 v63, v63, v65
	v_cvt_f16_f32_e32 v63, v63
	v_lshl_add_u32 v64, s34, 5, v117
	ds_write_b16 v64, v63
	s_branch .LBB0_73
